# MoE grouped GEMMs expert-major unit order (units of one expert contiguous: same-pn row tiles adjacent share weights, same-rt column tiles share gathered rows in one XCD L2)
# speedup vs baseline: 1.0079x; 1.0079x over previous
.LBB0_717:
	s_cmp_lt_i32 s76, s43
	s_cselect_b32 s45, s76, s44
	s_cmp_lt_i32 s45, 0
	s_cbranch_scc1 .LBB0_741
	s_add_u32 s8, s10, 0x1cd90000
	s_addc_u32 s9, s11, 0
	s_add_u32 s46, s10, 0x3adc0000
	s_addc_u32 s47, s11, 0
	s_abs_i32 s48, s42
	v_cvt_f32_u32_e32 v1, s48
	s_sub_i32 s2, 0, s48
	s_abs_i32 s1, s45
	s_ashr_i32 s0, s45, 31
	v_rcp_iflag_f32_e32 v1, v1
	s_ashr_i32 s49, s42, 31
	s_lshr_b32 s5, s4, 6
	s_xor_b32 s0, s0, s49
	v_mul_f32_e32 v1, 0x4f7ffffe, v1
	v_cvt_u32_f32_e32 v1, v1
	v_bfe_u32 v3, v0, 2, 4
	v_lshrrev_b32_e32 v4, 3, v0
	s_movk_i32 s61, 0x81
	v_readfirstlane_b32 s50, v1
	s_mul_i32 s2, s2, s50
	s_mul_hi_u32 s2, s50, s2
	s_add_i32 s50, s50, s2
	s_lshr_b32 s89, s45, 3
	s_lshl_b32 s89, s89, 2
	s_add_i32 s89, s89, 0x202e0
	v_mov_b32_e32 v222, s89
	ds_read_b32 v222, v222
	s_waitcnt lgkmcnt(0)
	v_lshlrev_b32_e32 v222, 2, v222
	v_add_u32_e32 v222, 0x20240, v222
	ds_read2_b32 v[252:253], v222 offset1:1
	s_waitcnt lgkmcnt(0)
	v_readfirstlane_b32 s90, v252
	v_readfirstlane_b32 s91, v253
	s_nop 3
	s_sub_i32 s91, s91, s90
	s_lshl_b32 s92, s90, 3
	s_sub_i32 s92, s45, s92
	s_mov_b32 s18, 0
	s_cmp_ge_u32 s92, s91
	s_cselect_b32 s93, s91, 0
	s_cselect_b32 s94, 1, 0
	s_sub_i32 s92, s92, s93
	s_add_i32 s18, s18, s94
	s_cmp_ge_u32 s92, s91
	s_cselect_b32 s93, s91, 0
	s_cselect_b32 s94, 1, 0
	s_sub_i32 s92, s92, s93
	s_add_i32 s18, s18, s94
	s_cmp_ge_u32 s92, s91
	s_cselect_b32 s93, s91, 0
	s_cselect_b32 s94, 1, 0
	s_sub_i32 s92, s92, s93
	s_add_i32 s18, s18, s94
	s_cmp_ge_u32 s92, s91
	s_cselect_b32 s93, s91, 0
	s_cselect_b32 s94, 1, 0
	s_sub_i32 s92, s92, s93
	s_add_i32 s18, s18, s94
	s_cmp_ge_u32 s92, s91
	s_cselect_b32 s93, s91, 0
	s_cselect_b32 s94, 1, 0
	s_sub_i32 s92, s92, s93
	s_add_i32 s18, s18, s94
	s_cmp_ge_u32 s92, s91
	s_cselect_b32 s93, s91, 0
	s_cselect_b32 s94, 1, 0
	s_sub_i32 s92, s92, s93
	s_add_i32 s18, s18, s94
	s_cmp_ge_u32 s92, s91
	s_cselect_b32 s93, s91, 0
	s_cselect_b32 s94, 1, 0
	s_sub_i32 s92, s92, s93
	s_add_i32 s18, s18, s94
	s_add_i32 s12, s90, s92
	s_lshl_b32 s0, s12, 2
	s_add_i32 s0, s0, 0
	s_add_i32 s0, s0, 0x202e0
	v_mov_b32_e32 v1, s0
	ds_read_b32 v5, v1
	v_and_or_b32 v1, v4, 48, v3
	v_or_b32_e32 v4, 64, v4
	s_movk_i32 s0, 0x70
	v_and_or_b32 v186, v4, s0, v3
	s_waitcnt lgkmcnt(0)
	v_lshlrev_b32_e32 v3, 2, v5
	v_add_u32_e32 v3, 0, v3
	v_add_u32_e32 v4, 0x20240, v3
	ds_read_b32 v4, v4
	v_add_u32_e32 v3, 0x201c0, v3
	ds_read_b32 v3, v3
	v_readfirstlane_b32 s2, v5
	s_ashr_i32 s3, s2, 31
	s_waitcnt lgkmcnt(1)
	v_sub_u32_e32 v4, s12, v4
	v_lshlrev_b32_e32 v18, 8, v4
	v_lshlrev_b32_e32 v4, 6, v5
	s_waitcnt lgkmcnt(0)
	v_add_u32_e32 v19, -1, v3
	v_add_u32_e32 v4, 0, v4
	v_or_b32_e32 v22, v18, v1
	v_add_u32_e32 v20, 0x208e0, v4
	v_min_i32_e32 v22, v22, v19
	ds_read2_b32 v[4:5], v20 offset0:1 offset1:2
	ds_read2_b32 v[6:7], v20 offset0:3 offset1:4
	ds_read2_b32 v[8:9], v20 offset0:5 offset1:6
	ds_read2_b32 v[10:11], v20 offset0:7 offset1:8
	ds_read2_b32 v[12:13], v20 offset0:9 offset1:10
	ds_read2_b32 v[14:15], v20 offset0:11 offset1:12
	ds_read2_b32 v[16:17], v20 offset0:13 offset1:14
	ds_read_b32 v21, v20 offset:60
	s_waitcnt lgkmcnt(7)
	v_cmp_ge_i32_e32 vcc, v22, v4
	v_or_b32_e32 v25, v18, v186
	v_min_i32_e32 v25, v25, v19
	v_cndmask_b32_e64 v23, 0, 1, vcc
	v_cmp_ge_i32_e32 vcc, v22, v5
	v_or_b32_e32 v28, 0x80, v18
	v_or_b32_e32 v29, v28, v1
	v_cndmask_b32_e64 v24, 0, 1, vcc
	s_waitcnt lgkmcnt(6)
	v_cmp_ge_i32_e32 vcc, v22, v6
	v_min_i32_e32 v29, v29, v19
	v_or_b32_e32 v28, v28, v186
	v_addc_co_u32_e32 v23, vcc, v23, v24, vcc
	v_cmp_ge_i32_e32 vcc, v22, v7
	v_min_i32_e32 v19, v28, v19
	s_lshl_b64 s[0:1], s[2:3], 15
	v_cndmask_b32_e64 v24, 0, 1, vcc
	s_waitcnt lgkmcnt(5)
	v_cmp_ge_i32_e32 vcc, v22, v8
	s_add_u32 s0, s46, s0
	s_addc_u32 s1, s47, s1
	v_addc_co_u32_e32 v23, vcc, v23, v24, vcc
	v_cmp_ge_i32_e32 vcc, v22, v9
	v_sub_u32_e32 v3, v3, v18
	s_nop 0
	v_cndmask_b32_e64 v24, 0, 1, vcc
	s_waitcnt lgkmcnt(4)
	v_cmp_ge_i32_e32 vcc, v22, v10
	s_nop 1
	v_addc_co_u32_e32 v23, vcc, v23, v24, vcc
	v_cmp_ge_i32_e32 vcc, v22, v11
	s_nop 1
	v_cndmask_b32_e64 v24, 0, 1, vcc
	s_waitcnt lgkmcnt(3)
	v_cmp_ge_i32_e32 vcc, v22, v12
	s_nop 1
	v_addc_co_u32_e32 v23, vcc, v23, v24, vcc
	v_cmp_ge_i32_e32 vcc, v22, v13
	s_nop 1
	v_cndmask_b32_e64 v24, 0, 1, vcc
	s_waitcnt lgkmcnt(2)
	v_cmp_ge_i32_e32 vcc, v22, v14
	s_nop 1
	v_addc_co_u32_e32 v23, vcc, v23, v24, vcc
	v_cmp_ge_i32_e32 vcc, v22, v15
	s_nop 1
	v_cndmask_b32_e64 v24, 0, 1, vcc
	s_waitcnt lgkmcnt(1)
	v_cmp_ge_i32_e32 vcc, v22, v16
	s_nop 1
	v_addc_co_u32_e32 v23, vcc, v23, v24, vcc
	v_cmp_ge_i32_e32 vcc, v22, v17
	s_nop 1
	v_cndmask_b32_e64 v24, 0, 1, vcc
	s_waitcnt lgkmcnt(0)
	v_cmp_ge_i32_e32 vcc, v22, v21
	s_nop 1
	v_addc_co_u32_e32 v23, vcc, v23, v24, vcc
	v_cmp_ge_i32_e32 vcc, v25, v4
	v_lshl_add_u32 v24, v23, 2, v20
	ds_read_b32 v24, v24
	v_cndmask_b32_e64 v26, 0, 1, vcc
	v_cmp_ge_i32_e32 vcc, v25, v5
	s_nop 1
	v_cndmask_b32_e64 v27, 0, 1, vcc
	v_cmp_ge_i32_e32 vcc, v25, v6
	s_nop 1
	v_addc_co_u32_e32 v26, vcc, v26, v27, vcc
	v_cmp_ge_i32_e32 vcc, v25, v7
	s_nop 1
	v_cndmask_b32_e64 v27, 0, 1, vcc
	v_cmp_ge_i32_e32 vcc, v25, v8
	s_nop 1
	v_addc_co_u32_e32 v26, vcc, v26, v27, vcc
	v_cmp_ge_i32_e32 vcc, v25, v9
	s_nop 1
	v_cndmask_b32_e64 v27, 0, 1, vcc
	v_cmp_ge_i32_e32 vcc, v25, v10
	s_nop 1
	v_addc_co_u32_e32 v26, vcc, v26, v27, vcc
	v_cmp_ge_i32_e32 vcc, v25, v11
	s_nop 1
	v_cndmask_b32_e64 v27, 0, 1, vcc
	v_cmp_ge_i32_e32 vcc, v25, v12
	s_nop 1
	v_addc_co_u32_e32 v26, vcc, v26, v27, vcc
	v_cmp_ge_i32_e32 vcc, v25, v13
	s_nop 1
	v_cndmask_b32_e64 v27, 0, 1, vcc
	v_cmp_ge_i32_e32 vcc, v25, v14
	s_nop 1
	v_addc_co_u32_e32 v26, vcc, v26, v27, vcc
	v_cmp_ge_i32_e32 vcc, v25, v15
	s_nop 1
	v_cndmask_b32_e64 v27, 0, 1, vcc
	v_cmp_ge_i32_e32 vcc, v25, v16
	s_nop 1
	v_addc_co_u32_e32 v26, vcc, v26, v27, vcc
	v_cmp_ge_i32_e32 vcc, v25, v17
	s_nop 1
	v_cndmask_b32_e64 v27, 0, 1, vcc
	v_cmp_ge_i32_e32 vcc, v25, v21
	s_nop 1
	v_addc_co_u32_e32 v26, vcc, v26, v27, vcc
	v_cmp_ge_i32_e32 vcc, v29, v4
	v_lshl_add_u32 v27, v26, 2, v20
	s_nop 0
	v_cndmask_b32_e64 v30, 0, 1, vcc
	v_cmp_ge_i32_e32 vcc, v29, v5
	s_nop 1
	v_cndmask_b32_e64 v31, 0, 1, vcc
	v_cmp_ge_i32_e32 vcc, v29, v6
	s_nop 1
	v_addc_co_u32_e32 v30, vcc, v30, v31, vcc
	v_cmp_ge_i32_e32 vcc, v29, v7
	s_nop 1
	v_cndmask_b32_e64 v31, 0, 1, vcc
	v_cmp_ge_i32_e32 vcc, v29, v8
	s_nop 1
	v_addc_co_u32_e32 v30, vcc, v30, v31, vcc
	v_cmp_ge_i32_e32 vcc, v29, v9
	s_nop 1
	v_cndmask_b32_e64 v31, 0, 1, vcc
	v_cmp_ge_i32_e32 vcc, v29, v10
	s_nop 1
	v_addc_co_u32_e32 v30, vcc, v30, v31, vcc
	v_cmp_ge_i32_e32 vcc, v29, v11
	s_nop 1
	v_cndmask_b32_e64 v31, 0, 1, vcc
	v_cmp_ge_i32_e32 vcc, v29, v12
	s_nop 1
	v_addc_co_u32_e32 v30, vcc, v30, v31, vcc
	v_cmp_ge_i32_e32 vcc, v29, v13
	s_nop 1
	v_cndmask_b32_e64 v31, 0, 1, vcc
	v_cmp_ge_i32_e32 vcc, v29, v14
	s_nop 1
	v_addc_co_u32_e32 v30, vcc, v30, v31, vcc
	v_cmp_ge_i32_e32 vcc, v29, v15
	s_nop 1
	v_cndmask_b32_e64 v31, 0, 1, vcc
	v_cmp_ge_i32_e32 vcc, v29, v16
	s_nop 1
	v_addc_co_u32_e32 v30, vcc, v30, v31, vcc
	v_cmp_ge_i32_e32 vcc, v29, v17
	s_nop 1
	v_cndmask_b32_e64 v31, 0, 1, vcc
	v_cmp_ge_i32_e32 vcc, v29, v21
	s_nop 1
	v_addc_co_u32_e32 v30, vcc, v30, v31, vcc
	v_cmp_ge_i32_e32 vcc, v19, v4
	v_lshl_add_u32 v31, v30, 2, v20
	s_nop 0
	v_cndmask_b32_e64 v4, 0, 1, vcc
	v_cmp_ge_i32_e32 vcc, v19, v5
	s_nop 1
	v_cndmask_b32_e64 v5, 0, 1, vcc
	v_cmp_ge_i32_e32 vcc, v19, v6
	s_nop 1
	v_addc_co_u32_e32 v4, vcc, v4, v5, vcc
	v_cmp_ge_i32_e32 vcc, v19, v7
	s_nop 1
	v_cndmask_b32_e64 v5, 0, 1, vcc
	v_cmp_ge_i32_e32 vcc, v19, v8
	s_nop 1
	v_addc_co_u32_e32 v4, vcc, v4, v5, vcc
	v_cmp_ge_i32_e32 vcc, v19, v9
	s_nop 1
	v_cndmask_b32_e64 v5, 0, 1, vcc
	v_cmp_ge_i32_e32 vcc, v19, v10
	s_nop 1
	v_addc_co_u32_e32 v4, vcc, v4, v5, vcc
	v_cmp_ge_i32_e32 vcc, v19, v11
	s_nop 1
	v_cndmask_b32_e64 v5, 0, 1, vcc
	v_cmp_ge_i32_e32 vcc, v19, v12
	s_nop 1
	v_addc_co_u32_e32 v4, vcc, v4, v5, vcc
	v_cmp_ge_i32_e32 vcc, v19, v13
	s_nop 1
	v_cndmask_b32_e64 v5, 0, 1, vcc
	v_cmp_ge_i32_e32 vcc, v19, v14
	s_nop 1
	v_addc_co_u32_e32 v4, vcc, v4, v5, vcc
	v_cmp_ge_i32_e32 vcc, v19, v15
	s_nop 1
	v_cndmask_b32_e64 v5, 0, 1, vcc
	v_cmp_ge_i32_e32 vcc, v19, v16
	s_nop 1
	v_addc_co_u32_e32 v4, vcc, v4, v5, vcc
	v_cmp_ge_i32_e32 vcc, v19, v17
	s_nop 1
	v_cndmask_b32_e64 v5, 0, 1, vcc
	v_cmp_ge_i32_e32 vcc, v19, v21
	s_nop 1
	v_addc_co_u32_e32 v8, vcc, v4, v5, vcc
	v_lshl_add_u32 v4, v8, 2, v20
	ds_read_b32 v6, v27
	ds_read_b32 v9, v31
	ds_read_b32 v10, v4
	s_waitcnt lgkmcnt(3)
	v_sub_u32_e32 v4, v22, v24
	v_lshl_add_u32 v4, v23, 9, v4
	s_waitcnt lgkmcnt(2)
	v_sub_u32_e32 v6, v25, v6
	v_ashrrev_i32_e32 v5, 31, v4
	v_lshl_add_u32 v6, v26, 9, v6
	v_lshl_add_u64 v[4:5], v[4:5], 2, s[0:1]
	v_ashrrev_i32_e32 v7, 31, v6
	v_lshl_add_u64 v[6:7], v[6:7], 2, s[0:1]
	global_load_dword v11, v[4:5], off
	global_load_dword v12, v[6:7], off
	v_lshlrev_b32_e32 v4, 4, v0
	v_and_b32_e32 v5, 32, v0
	v_bitop3_b32 v4, v4, v5, 48 bitop3:0x6c
	v_and_or_b32 v187, v0, 64, v4
	s_waitcnt lgkmcnt(1)
	v_sub_u32_e32 v4, v29, v9
	v_lshl_add_u32 v6, v8, 9, v19
	v_lshl_add_u32 v4, v30, 9, v4
	s_waitcnt lgkmcnt(0)
	v_sub_u32_e32 v6, v6, v10
	v_ashrrev_i32_e32 v5, 31, v4
	v_ashrrev_i32_e32 v7, 31, v6
	v_lshl_add_u64 v[4:5], v[4:5], 2, s[0:1]
	v_lshl_add_u64 v[6:7], v[6:7], 2, s[0:1]
	s_lshl_b32 s0, s5, 10
	global_load_dword v8, v[4:5], off
	global_load_dword v9, v[6:7], off
	s_waitcnt vmcnt(0)
	s_add_i32 s51, s0, 0
	s_waitcnt lgkmcnt(0)
	s_barrier
	s_mov_b32 m0, s51
	s_add_i32 s60, s51, 0x2000
	v_cmp_gt_i32_e64 s[0:1], s61, v3
	s_and_b64 vcc, exec, s[0:1]
	s_waitcnt vmcnt(3)
	v_lshl_or_b32 v178, v11, 12, v187
	s_waitcnt vmcnt(2)
	v_lshl_or_b32 v180, v12, 12, v187
	global_load_lds_dwordx4 v178, s[8:9]
	s_mov_b32 m0, s60
	s_waitcnt vmcnt(0)
	v_lshl_or_b32 v182, v8, 12, v187
	global_load_lds_dwordx4 v180, s[8:9]
	v_lshl_or_b32 v184, v9, 12, v187
	s_cbranch_vccnz .LBB0_720
	s_add_i32 m0, s51, 0x4000
	s_nop 0
	global_load_lds_dwordx4 v182, s[8:9]
	s_add_i32 m0, s51, 0x6000
	s_nop 0
	global_load_lds_dwordx4 v184, s[8:9]

.LBB0_721:
	s_add_i32 s0, s45, s33
	s_cmp_lt_i32 s45, s43
	s_cselect_b32 s1, s44, -1
	s_cmp_lt_i32 s0, s43
	s_cselect_b32 s45, s0, s1
	s_cmp_lt_i32 s45, 0
	s_cselect_b64 s[14:15], -1, 0
	s_and_b64 vcc, exec, s[14:15]
	v_mov_b32_e32 v209, v178
	v_mov_b32_e32 v210, v180
	v_mov_b32_e32 v211, v182
	v_mov_b32_e32 v212, v184
	s_mov_b32 s16, s18
	s_cbranch_vccnz .LBB0_723
	s_lshr_b32 s89, s45, 3
	s_lshl_b32 s89, s89, 2
	s_add_i32 s89, s89, 0x202e0
	v_mov_b32_e32 v222, s89
	ds_read_b32 v222, v222
	s_waitcnt lgkmcnt(0)
	v_lshlrev_b32_e32 v222, 2, v222
	v_add_u32_e32 v222, 0x20240, v222
	ds_read2_b32 v[252:253], v222 offset1:1
	s_waitcnt lgkmcnt(0)
	v_readfirstlane_b32 s90, v252
	v_readfirstlane_b32 s91, v253
	s_nop 3
	s_sub_i32 s91, s91, s90
	s_lshl_b32 s92, s90, 3
	s_sub_i32 s92, s45, s92
	s_mov_b32 s16, 0
	s_cmp_ge_u32 s92, s91
	s_cselect_b32 s93, s91, 0
	s_cselect_b32 s94, 1, 0
	s_sub_i32 s92, s92, s93
	s_add_i32 s16, s16, s94
	s_cmp_ge_u32 s92, s91
	s_cselect_b32 s93, s91, 0
	s_cselect_b32 s94, 1, 0
	s_sub_i32 s92, s92, s93
	s_add_i32 s16, s16, s94
	s_cmp_ge_u32 s92, s91
	s_cselect_b32 s93, s91, 0
	s_cselect_b32 s94, 1, 0
	s_sub_i32 s92, s92, s93
	s_add_i32 s16, s16, s94
	s_cmp_ge_u32 s92, s91
	s_cselect_b32 s93, s91, 0
	s_cselect_b32 s94, 1, 0
	s_sub_i32 s92, s92, s93
	s_add_i32 s16, s16, s94
	s_cmp_ge_u32 s92, s91
	s_cselect_b32 s93, s91, 0
	s_cselect_b32 s94, 1, 0
	s_sub_i32 s92, s92, s93
	s_add_i32 s16, s16, s94
	s_cmp_ge_u32 s92, s91
	s_cselect_b32 s93, s91, 0
	s_cselect_b32 s94, 1, 0
	s_sub_i32 s92, s92, s93
	s_add_i32 s16, s16, s94
	s_cmp_ge_u32 s92, s91
	s_cselect_b32 s93, s91, 0
	s_cselect_b32 s94, 1, 0
	s_sub_i32 s92, s92, s93
	s_add_i32 s16, s16, s94
	s_add_i32 s4, s90, s92
	s_lshl_b32 s0, s4, 2
	s_add_i32 s0, s0, 0
	s_add_i32 s0, s0, 0x202e0
	v_mov_b32_e32 v30, s0
	ds_read_b32 v30, v30
	s_ashr_i32 s17, s16, 31
	s_waitcnt lgkmcnt(0)
	v_lshlrev_b32_e32 v31, 2, v30
	v_add_u32_e32 v31, 0, v31
	v_add_u32_e32 v32, 0x20240, v31
	ds_read_b32 v32, v32
	v_add_u32_e32 v31, 0x201c0, v31
	ds_read_b32 v48, v31
	v_readfirstlane_b32 s2, v30
	v_lshlrev_b32_e32 v30, 6, v30
	s_waitcnt lgkmcnt(0)
	v_sub_u32_e32 v31, s4, v32
	v_lshlrev_b32_e32 v49, 8, v31
	v_add_u32_e32 v50, -1, v48
	v_add_u32_e32 v30, 0, v30
	v_or_b32_e32 v53, v49, v1
	v_add_u32_e32 v51, 0x208e0, v30
	v_min_i32_e32 v53, v53, v50
	ds_read2_b32 v[30:31], v51 offset0:1 offset1:2
	ds_read2_b32 v[32:33], v51 offset0:3 offset1:4
	ds_read2_b32 v[38:39], v51 offset0:5 offset1:6
	ds_read2_b32 v[40:41], v51 offset0:7 offset1:8
	ds_read2_b32 v[42:43], v51 offset0:9 offset1:10
	ds_read2_b32 v[44:45], v51 offset0:11 offset1:12
	ds_read2_b32 v[46:47], v51 offset0:13 offset1:14
	ds_read_b32 v52, v51 offset:60
	s_waitcnt lgkmcnt(0)
	v_cmp_ge_i32_e32 vcc, v53, v30
	v_or_b32_e32 v56, v49, v186
	v_min_i32_e32 v56, v56, v50
	v_cndmask_b32_e64 v54, 0, 1, vcc
	v_cmp_ge_i32_e32 vcc, v53, v31
	v_or_b32_e32 v59, 0x80, v49
	v_or_b32_e32 v60, v59, v1
	v_cndmask_b32_e64 v55, 0, 1, vcc
	v_cmp_ge_i32_e32 vcc, v53, v32
	v_min_i32_e32 v60, v60, v50
	v_or_b32_e32 v59, v59, v186
	v_addc_co_u32_e32 v54, vcc, v54, v55, vcc
	v_cmp_ge_i32_e32 vcc, v53, v33
	v_min_i32_e32 v50, v59, v50
	s_ashr_i32 s3, s2, 31
	v_cndmask_b32_e64 v55, 0, 1, vcc
	v_cmp_ge_i32_e32 vcc, v53, v38
	s_lshl_b64 s[0:1], s[2:3], 23
	s_add_u32 s5, s52, s0
	v_addc_co_u32_e32 v54, vcc, v54, v55, vcc
	v_cmp_ge_i32_e32 vcc, v53, v39
	s_addc_u32 s23, s53, s1
	s_lshl_b64 s[2:3], s[2:3], 15
	v_cndmask_b32_e64 v55, 0, 1, vcc
	v_cmp_ge_i32_e32 vcc, v53, v40
	s_add_u32 s2, s46, s2
	s_addc_u32 s3, s47, s3
	v_addc_co_u32_e32 v54, vcc, v54, v55, vcc
	v_cmp_ge_i32_e32 vcc, v53, v41
	s_lshl_b32 s64, s4, 8
	s_nop 0
	v_cndmask_b32_e64 v55, 0, 1, vcc
	v_cmp_ge_i32_e32 vcc, v53, v42
	s_nop 1
	v_addc_co_u32_e32 v54, vcc, v54, v55, vcc
	v_cmp_ge_i32_e32 vcc, v53, v43
	s_nop 1
	v_cndmask_b32_e64 v55, 0, 1, vcc
	v_cmp_ge_i32_e32 vcc, v53, v44
	s_nop 1
	v_addc_co_u32_e32 v54, vcc, v54, v55, vcc
	v_cmp_ge_i32_e32 vcc, v53, v45
	s_nop 1
	v_cndmask_b32_e64 v55, 0, 1, vcc
	v_cmp_ge_i32_e32 vcc, v53, v46
	s_nop 1
	v_addc_co_u32_e32 v54, vcc, v54, v55, vcc
	v_cmp_ge_i32_e32 vcc, v53, v47
	s_nop 1
	v_cndmask_b32_e64 v55, 0, 1, vcc
	v_cmp_ge_i32_e32 vcc, v53, v52
	s_nop 1
	v_addc_co_u32_e32 v54, vcc, v54, v55, vcc
	v_cmp_ge_i32_e32 vcc, v56, v30
	v_lshl_add_u32 v55, v54, 2, v51
	ds_read_b32 v55, v55
	v_cndmask_b32_e64 v57, 0, 1, vcc
	v_cmp_ge_i32_e32 vcc, v56, v31
	s_nop 1
	v_cndmask_b32_e64 v58, 0, 1, vcc
	v_cmp_ge_i32_e32 vcc, v56, v32
	s_nop 1
	v_addc_co_u32_e32 v57, vcc, v57, v58, vcc
	v_cmp_ge_i32_e32 vcc, v56, v33
	s_nop 1
	v_cndmask_b32_e64 v58, 0, 1, vcc
	v_cmp_ge_i32_e32 vcc, v56, v38
	s_nop 1
	v_addc_co_u32_e32 v57, vcc, v57, v58, vcc
	v_cmp_ge_i32_e32 vcc, v56, v39
	s_nop 1
	v_cndmask_b32_e64 v58, 0, 1, vcc
	v_cmp_ge_i32_e32 vcc, v56, v40
	s_nop 1
	v_addc_co_u32_e32 v57, vcc, v57, v58, vcc
	v_cmp_ge_i32_e32 vcc, v56, v41
	s_nop 1
	v_cndmask_b32_e64 v58, 0, 1, vcc
	v_cmp_ge_i32_e32 vcc, v56, v42
	s_nop 1
	v_addc_co_u32_e32 v57, vcc, v57, v58, vcc
	v_cmp_ge_i32_e32 vcc, v56, v43
	s_nop 1
	v_cndmask_b32_e64 v58, 0, 1, vcc
	v_cmp_ge_i32_e32 vcc, v56, v44
	s_nop 1
	v_addc_co_u32_e32 v57, vcc, v57, v58, vcc
	v_cmp_ge_i32_e32 vcc, v56, v45
	s_nop 1
	v_cndmask_b32_e64 v58, 0, 1, vcc
	v_cmp_ge_i32_e32 vcc, v56, v46
	s_nop 1
	v_addc_co_u32_e32 v57, vcc, v57, v58, vcc
	v_cmp_ge_i32_e32 vcc, v56, v47
	s_nop 1
	v_cndmask_b32_e64 v58, 0, 1, vcc
	v_cmp_ge_i32_e32 vcc, v56, v52
	s_nop 1
	v_addc_co_u32_e32 v57, vcc, v57, v58, vcc
	v_cmp_ge_i32_e32 vcc, v60, v30
	v_lshl_add_u32 v58, v57, 2, v51
	s_nop 0
	v_cndmask_b32_e64 v61, 0, 1, vcc
	v_cmp_ge_i32_e32 vcc, v60, v31
	s_nop 1
	v_cndmask_b32_e64 v62, 0, 1, vcc
	v_cmp_ge_i32_e32 vcc, v60, v32
	s_nop 1
	v_addc_co_u32_e32 v61, vcc, v61, v62, vcc
	v_cmp_ge_i32_e32 vcc, v60, v33
	s_nop 1
	v_cndmask_b32_e64 v62, 0, 1, vcc
	v_cmp_ge_i32_e32 vcc, v60, v38
	s_nop 1
	v_addc_co_u32_e32 v61, vcc, v61, v62, vcc
	v_cmp_ge_i32_e32 vcc, v60, v39
	s_nop 1
	v_cndmask_b32_e64 v62, 0, 1, vcc
	v_cmp_ge_i32_e32 vcc, v60, v40
	s_nop 1
	v_addc_co_u32_e32 v61, vcc, v61, v62, vcc
	v_cmp_ge_i32_e32 vcc, v60, v41
	s_nop 1
	v_cndmask_b32_e64 v62, 0, 1, vcc
	v_cmp_ge_i32_e32 vcc, v60, v42
	s_nop 1
	v_addc_co_u32_e32 v61, vcc, v61, v62, vcc
	v_cmp_ge_i32_e32 vcc, v60, v43
	s_nop 1
	v_cndmask_b32_e64 v62, 0, 1, vcc
	v_cmp_ge_i32_e32 vcc, v60, v44
	s_nop 1
	v_addc_co_u32_e32 v61, vcc, v61, v62, vcc
	v_cmp_ge_i32_e32 vcc, v60, v45
	s_nop 1
	v_cndmask_b32_e64 v62, 0, 1, vcc
	v_cmp_ge_i32_e32 vcc, v60, v46
	s_nop 1
	v_addc_co_u32_e32 v61, vcc, v61, v62, vcc
	v_cmp_ge_i32_e32 vcc, v60, v47
	s_nop 1
	v_cndmask_b32_e64 v62, 0, 1, vcc
	v_cmp_ge_i32_e32 vcc, v60, v52
	s_nop 1
	v_addc_co_u32_e32 v61, vcc, v61, v62, vcc
	v_cmp_ge_i32_e32 vcc, v50, v30
	v_lshl_add_u32 v62, v61, 2, v51
	s_nop 0
	v_cndmask_b32_e64 v30, 0, 1, vcc
	v_cmp_ge_i32_e32 vcc, v50, v31
	s_nop 1
	v_cndmask_b32_e64 v31, 0, 1, vcc
	v_cmp_ge_i32_e32 vcc, v50, v32
	s_nop 1
	v_addc_co_u32_e32 v30, vcc, v30, v31, vcc
	v_cmp_ge_i32_e32 vcc, v50, v33
	s_nop 1
	v_cndmask_b32_e64 v31, 0, 1, vcc
	v_cmp_ge_i32_e32 vcc, v50, v38
	s_nop 1
	v_addc_co_u32_e32 v30, vcc, v30, v31, vcc
	v_cmp_ge_i32_e32 vcc, v50, v39
	s_nop 1
	v_cndmask_b32_e64 v31, 0, 1, vcc
	v_cmp_ge_i32_e32 vcc, v50, v40
	s_nop 1
	v_addc_co_u32_e32 v30, vcc, v30, v31, vcc
	v_cmp_ge_i32_e32 vcc, v50, v41
	s_nop 1
	v_cndmask_b32_e64 v31, 0, 1, vcc
	v_cmp_ge_i32_e32 vcc, v50, v42
	s_nop 1
	v_addc_co_u32_e32 v30, vcc, v30, v31, vcc
	v_cmp_ge_i32_e32 vcc, v50, v43
	s_nop 1
	v_cndmask_b32_e64 v31, 0, 1, vcc
	v_cmp_ge_i32_e32 vcc, v50, v44
	s_nop 1
	v_addc_co_u32_e32 v30, vcc, v30, v31, vcc
	v_cmp_ge_i32_e32 vcc, v50, v45
	s_nop 1
	v_cndmask_b32_e64 v31, 0, 1, vcc
	v_cmp_ge_i32_e32 vcc, v50, v46
	s_nop 1
	v_addc_co_u32_e32 v30, vcc, v30, v31, vcc
	v_cmp_ge_i32_e32 vcc, v50, v47
	s_nop 1
	v_cndmask_b32_e64 v31, 0, 1, vcc
	v_cmp_ge_i32_e32 vcc, v50, v52
	s_nop 1
	v_addc_co_u32_e32 v40, vcc, v30, v31, vcc
	v_lshl_add_u32 v30, v40, 2, v51
	ds_read_b32 v32, v58
	ds_read_b32 v38, v62
	ds_read_b32 v41, v30
	s_waitcnt lgkmcnt(0)
	v_sub_u32_e32 v30, v53, v55
	v_lshl_add_u32 v30, v54, 9, v30
	v_sub_u32_e32 v32, v56, v32
	v_lshl_add_u32 v32, v57, 9, v32
	v_sub_u32_e32 v38, v60, v38
	v_lshl_add_u32 v40, v40, 9, v50
	v_ashrrev_i32_e32 v31, 31, v30
	v_ashrrev_i32_e32 v33, 31, v32
	v_lshl_add_u32 v38, v61, 9, v38
	v_sub_u32_e32 v40, v40, v41
	v_lshl_add_u64 v[30:31], v[30:31], 2, s[2:3]
	v_lshl_add_u64 v[32:33], v[32:33], 2, s[2:3]
	v_ashrrev_i32_e32 v39, 31, v38
	v_ashrrev_i32_e32 v41, 31, v40
	v_lshl_add_u64 v[38:39], v[38:39], 2, s[2:3]
	v_lshl_add_u64 v[40:41], v[40:41], 2, s[2:3]
	global_load_dword v30, v[30:31], off
	s_nop 0
	global_load_dword v31, v[32:33], off
	s_nop 0
	global_load_dword v32, v[38:39], off
	global_load_dword v33, v[40:41], off
	s_add_u32 s2, s26, s0
	s_addc_u32 s3, s27, s1
	s_lshl_b64 s[0:1], s[16:17], 9
	s_add_u32 s20, s2, s0
	v_sub_u32_e32 v38, v48, v49
	s_addc_u32 s21, s3, s1
	v_cmp_gt_i32_e32 vcc, s61, v38
	s_add_u32 s22, s5, s0
	s_addc_u32 s23, s23, s1
	v_cndmask_b32_e64 v208, 0, 1, vcc
	s_waitcnt vmcnt(0)
	v_lshl_or_b32 v209, v30, 12, v187
	v_lshl_or_b32 v210, v31, 12, v187
	v_lshl_or_b32 v211, v32, 12, v187
	v_lshl_or_b32 v212, v33, 12, v187

.LBB0_849:
	s_cmp_lt_i32 s76, s53
	s_cselect_b32 s61, s76, s60
	s_cmp_lt_i32 s61, 0
	s_cbranch_scc1 .LBB0_873
	s_add_u32 s62, s10, 0x1ed90000
	s_addc_u32 s63, s11, 0
	s_abs_i32 s64, s52
	v_cvt_f32_u32_e32 v4, s64
	s_sub_i32 s2, 0, s64
	s_abs_i32 s1, s61
	s_ashr_i32 s0, s61, 31
	v_rcp_iflag_f32_e32 v4, v4
	s_ashr_i32 s65, s52, 31
	s_lshr_b32 s9, s8, 6
	s_xor_b32 s0, s0, s65
	v_mul_f32_e32 v4, 0x4f7ffffe, v4
	v_cvt_u32_f32_e32 v4, v4
	v_lshlrev_b32_e32 v1, 4, v0
	v_and_b32_e32 v2, 32, v0
	v_bfe_u32 v3, v0, 2, 4
	v_readfirstlane_b32 s66, v4
	s_mul_i32 s2, s2, s66
	s_mul_hi_u32 s2, s66, s2
	s_add_i32 s66, s66, s2
	s_lshr_b32 s89, s61, 3
	s_lshl_b32 s89, s89, 2
	s_add_i32 s89, s89, 0x202e0
	v_mov_b32_e32 v222, s89
	ds_read_b32 v222, v222
	s_waitcnt lgkmcnt(0)
	v_lshlrev_b32_e32 v222, 2, v222
	v_add_u32_e32 v222, 0x20240, v222
	ds_read2_b32 v[252:253], v222 offset1:1
	s_waitcnt lgkmcnt(0)
	v_readfirstlane_b32 s90, v252
	v_readfirstlane_b32 s91, v253
	s_nop 3
	s_sub_i32 s91, s91, s90
	s_lshl_b32 s92, s90, 3
	s_sub_i32 s92, s61, s92
	s_mov_b32 s18, 0
	s_cmp_ge_u32 s92, s91
	s_cselect_b32 s93, s91, 0
	s_cselect_b32 s94, 1, 0
	s_sub_i32 s92, s92, s93
	s_add_i32 s18, s18, s94
	s_cmp_ge_u32 s92, s91
	s_cselect_b32 s93, s91, 0
	s_cselect_b32 s94, 1, 0
	s_sub_i32 s92, s92, s93
	s_add_i32 s18, s18, s94
	s_cmp_ge_u32 s92, s91
	s_cselect_b32 s93, s91, 0
	s_cselect_b32 s94, 1, 0
	s_sub_i32 s92, s92, s93
	s_add_i32 s18, s18, s94
	s_cmp_ge_u32 s92, s91
	s_cselect_b32 s93, s91, 0
	s_cselect_b32 s94, 1, 0
	s_sub_i32 s92, s92, s93
	s_add_i32 s18, s18, s94
	s_cmp_ge_u32 s92, s91
	s_cselect_b32 s93, s91, 0
	s_cselect_b32 s94, 1, 0
	s_sub_i32 s92, s92, s93
	s_add_i32 s18, s18, s94
	s_cmp_ge_u32 s92, s91
	s_cselect_b32 s93, s91, 0
	s_cselect_b32 s94, 1, 0
	s_sub_i32 s92, s92, s93
	s_add_i32 s18, s18, s94
	s_cmp_ge_u32 s92, s91
	s_cselect_b32 s93, s91, 0
	s_cselect_b32 s94, 1, 0
	s_sub_i32 s92, s92, s93
	s_add_i32 s18, s18, s94
	s_add_i32 s3, s90, s92
	s_lshl_b32 s0, s3, 2
	s_add_i32 s0, s0, 0
	s_add_i32 s0, s0, 0x202e0
	v_mov_b32_e32 v4, s0
	ds_read_b32 v4, v4
	v_bitop3_b32 v1, v1, v2, 48 bitop3:0x6c
	v_lshrrev_b32_e32 v2, 3, v0
	s_lshl_b32 s20, s3, 8
	v_and_or_b32 v5, v2, 48, v3
	v_or_b32_e32 v2, 64, v2
	s_movk_i32 s0, 0x70
	s_ashr_i32 s21, s20, 31
	v_and_or_b32 v2, v2, s0, v3
	s_waitcnt lgkmcnt(0)
	v_lshlrev_b32_e32 v3, 2, v4
	s_lshl_b64 s[0:1], s[20:21], 11
	v_add_u32_e32 v3, 0, v3
	s_add_u32 s22, s62, s0
	v_add_u32_e32 v6, 0x20240, v3
	v_add_u32_e32 v3, 0x201c0, v3
	s_addc_u32 s23, s63, s1
	s_lshl_b32 s0, s9, 10
	v_and_or_b32 v1, v0, 64, v1
	ds_read_b32 v6, v6
	ds_read_b32 v3, v3
	s_add_i32 s21, s0, 0
	s_waitcnt vmcnt(0)
	s_add_i32 s67, s21, 0x2000
	v_lshl_or_b32 v180, v5, 11, v1
	s_waitcnt lgkmcnt(0)
	s_barrier
	s_mov_b32 m0, s21
	v_lshl_or_b32 v182, v2, 11, v1
	global_load_lds_dwordx4 v180, s[22:23]
	s_mov_b32 m0, s67
	s_waitcnt lgkmcnt(0)
	v_subrev_u32_e32 v1, s3, v6
	global_load_lds_dwordx4 v182, s[22:23]
	v_lshlrev_b32_e32 v1, 8, v1
	v_add_u32_e32 v1, v1, v3
	s_movk_i32 s3, 0x80
	s_movk_i32 s0, 0x81
	v_cmp_lt_i32_e32 vcc, s3, v1
	v_mov_b32_e32 v187, 0
	v_readfirstlane_b32 s2, v4
	v_cmp_gt_i32_e64 s[0:1], s0, v1
	v_or_b32_e32 v184, 0x40000, v180
	v_or_b32_e32 v186, 0x40000, v182
	v_mov_b32_e32 v185, v187
	s_cbranch_vccz .LBB0_852
	s_add_i32 m0, s21, 0x4000
	v_lshl_add_u64 v[2:3], s[22:23], 0, v[186:187]
	global_load_lds_dwordx4 v184, s[22:23]
	s_add_i32 m0, s21, 0x6000
	s_nop 0
	global_load_lds_dwordx4 v[2:3], off

.LBB0_853:
	s_add_i32 s0, s61, s33
	s_cmp_lt_i32 s61, s53
	s_cselect_b32 s1, s60, -1
	s_cmp_lt_i32 s0, s53
	s_cselect_b32 s61, s0, s1
	s_cmp_lt_i32 s61, 0
	s_cselect_b64 s[24:25], -1, 0
	s_and_b64 vcc, exec, s[24:25]
	s_mov_b32 s36, s18
	s_mov_b32 s42, s20
	s_cbranch_vccnz .LBB0_855
	s_lshr_b32 s89, s61, 3
	s_lshl_b32 s89, s89, 2
	s_add_i32 s89, s89, 0x202e0
	v_mov_b32_e32 v222, s89
	ds_read_b32 v222, v222
	s_waitcnt lgkmcnt(0)
	v_lshlrev_b32_e32 v222, 2, v222
	v_add_u32_e32 v222, 0x20240, v222
	ds_read2_b32 v[252:253], v222 offset1:1
	s_waitcnt lgkmcnt(0)
	v_readfirstlane_b32 s90, v252
	v_readfirstlane_b32 s91, v253
	s_nop 3
	s_sub_i32 s91, s91, s90
	s_lshl_b32 s92, s90, 3
	s_sub_i32 s92, s61, s92
	s_mov_b32 s36, 0
	s_cmp_ge_u32 s92, s91
	s_cselect_b32 s93, s91, 0
	s_cselect_b32 s94, 1, 0
	s_sub_i32 s92, s92, s93
	s_add_i32 s36, s36, s94
	s_cmp_ge_u32 s92, s91
	s_cselect_b32 s93, s91, 0
	s_cselect_b32 s94, 1, 0
	s_sub_i32 s92, s92, s93
	s_add_i32 s36, s36, s94
	s_cmp_ge_u32 s92, s91
	s_cselect_b32 s93, s91, 0
	s_cselect_b32 s94, 1, 0
	s_sub_i32 s92, s92, s93
	s_add_i32 s36, s36, s94
	s_cmp_ge_u32 s92, s91
	s_cselect_b32 s93, s91, 0
	s_cselect_b32 s94, 1, 0
	s_sub_i32 s92, s92, s93
	s_add_i32 s36, s36, s94
	s_cmp_ge_u32 s92, s91
	s_cselect_b32 s93, s91, 0
	s_cselect_b32 s94, 1, 0
	s_sub_i32 s92, s92, s93
	s_add_i32 s36, s36, s94
	s_cmp_ge_u32 s92, s91
	s_cselect_b32 s93, s91, 0
	s_cselect_b32 s94, 1, 0
	s_sub_i32 s92, s92, s93
	s_add_i32 s36, s36, s94
	s_cmp_ge_u32 s92, s91
	s_cselect_b32 s93, s91, 0
	s_cselect_b32 s94, 1, 0
	s_sub_i32 s92, s92, s93
	s_add_i32 s36, s36, s94
	s_add_i32 s2, s90, s92
	s_lshl_b32 s0, s2, 2
	s_add_i32 s0, s0, 0
	s_add_i32 s0, s0, 0x202e0
	v_mov_b32_e32 v1, s0
	ds_read_b32 v1, v1
	s_ashr_i32 s37, s36, 31
	s_waitcnt lgkmcnt(0)
	v_lshlrev_b32_e32 v2, 2, v1
	v_add_u32_e32 v2, 0, v2
	v_readfirstlane_b32 s0, v1
	v_add_u32_e32 v3, 0x20240, v2
	s_ashr_i32 s1, s0, 31
	ds_read_b32 v3, v3
	s_lshl_b64 s[0:1], s[0:1], 23
	v_add_u32_e32 v2, 0x201c0, v2
	s_add_u32 s3, s54, s0
	ds_read_b32 v2, v2
	s_addc_u32 s27, s55, s1
	s_lshl_b32 s42, s2, 8
	s_lshl_b64 s[0:1], s[36:37], 10
	s_add_u32 s26, s3, s0
	s_addc_u32 s27, s27, s1
	s_waitcnt lgkmcnt(0)
	v_subrev_u32_e32 v1, s2, v3
	s_add_u32 s38, s26, 0x200
	v_lshlrev_b32_e32 v1, 8, v1
	s_addc_u32 s39, s27, 0
	s_ashr_i32 s43, s42, 31
	v_add_u32_e32 v1, v1, v2
	s_lshl_b64 s[0:1], s[42:43], 11
	v_cmp_gt_i32_e32 vcc, s19, v1
	s_add_u32 s40, s62, s0
	s_addc_u32 s41, s63, s1
	v_cndmask_b32_e64 v208, 0, 1, vcc

	.amdhsa_kernel _Z4mega4Args
		.amdhsa_group_segment_fixed_size 0
		.amdhsa_private_segment_fixed_size 0
		.amdhsa_kernarg_size 432
		.amdhsa_user_sgpr_count 2
		.amdhsa_user_sgpr_dispatch_ptr 0
		.amdhsa_user_sgpr_queue_ptr 0
		.amdhsa_user_sgpr_kernarg_segment_ptr 1
		.amdhsa_user_sgpr_dispatch_id 0
		.amdhsa_user_sgpr_kernarg_preload_length 0
		.amdhsa_user_sgpr_kernarg_preload_offset 0
		.amdhsa_user_sgpr_private_segment_size 0
		.amdhsa_uses_dynamic_stack 0
		.amdhsa_enable_private_segment 0
		.amdhsa_system_sgpr_workgroup_id_x 1
		.amdhsa_system_sgpr_workgroup_id_y 0
		.amdhsa_system_sgpr_workgroup_id_z 0
		.amdhsa_system_sgpr_workgroup_info 0
		.amdhsa_system_vgpr_workitem_id 0
		.amdhsa_next_free_vgpr 256
		.amdhsa_next_free_sgpr 102
		.amdhsa_accum_offset 256
		.amdhsa_reserve_vcc 1
		.amdhsa_float_round_mode_32 0
		.amdhsa_float_round_mode_16_64 0
		.amdhsa_float_denorm_mode_32 3
		.amdhsa_float_denorm_mode_16_64 3
		.amdhsa_dx10_clamp 1
		.amdhsa_ieee_mode 1
		.amdhsa_fp16_overflow 0
		.amdhsa_tg_split 0
		.amdhsa_exception_fp_ieee_invalid_op 0
		.amdhsa_exception_fp_denorm_src 0
		.amdhsa_exception_fp_ieee_div_zero 0
		.amdhsa_exception_fp_ieee_overflow 0
		.amdhsa_exception_fp_ieee_underflow 0
		.amdhsa_exception_fp_ieee_inexact 0
		.amdhsa_exception_int_div_zero 0
	.end_amdhsa_kernel

amdhsa.kernels:
  - .agpr_count:     0
    .args:
      - .offset:         0
        .size:           176
        .value_kind:     by_value
      - .offset:         176
        .size:           4
        .value_kind:     hidden_block_count_x
      - .offset:         180
        .size:           4
        .value_kind:     hidden_block_count_y
      - .offset:         184
        .size:           4
        .value_kind:     hidden_block_count_z
      - .offset:         188
        .size:           2
        .value_kind:     hidden_group_size_x
      - .offset:         190
        .size:           2
        .value_kind:     hidden_group_size_y
      - .offset:         192
        .size:           2
        .value_kind:     hidden_group_size_z
      - .offset:         194
        .size:           2
        .value_kind:     hidden_remainder_x
      - .offset:         196
        .size:           2
        .value_kind:     hidden_remainder_y
      - .offset:         198
        .size:           2
        .value_kind:     hidden_remainder_z
      - .offset:         216
        .size:           8
        .value_kind:     hidden_global_offset_x
      - .offset:         224
        .size:           8
        .value_kind:     hidden_global_offset_y
      - .offset:         232
        .size:           8
        .value_kind:     hidden_global_offset_z
      - .offset:         240
        .size:           2
        .value_kind:     hidden_grid_dims
      - .offset:         296
        .size:           4
        .value_kind:     hidden_dynamic_lds_size
    .group_segment_fixed_size: 0
    .kernarg_segment_align: 8
    .kernarg_segment_size: 432
    .language:       OpenCL C
    .language_version:
      - 2
      - 0
    .max_flat_workgroup_size: 512
    .name:           _Z4mega4Args
    .private_segment_fixed_size: 0
    .sgpr_count:     108
    .sgpr_spill_count: 7
    .symbol:         _Z4mega4Args.kd
    .uniform_work_group_size: 1
    .uses_dynamic_stack: false
    .vgpr_count:     256
    .vgpr_spill_count: 0
    .wavefront_size: 64
